# PEER expert sweeps: per-XCD starting-slice rotation removed (all XCDs sweep the column slices in the same order), on top of v16
# speedup vs baseline: 1.0003x; 1.0003x over previous
; #define LAS __attribute__((address_space(3)))
; __device__ __forceinline__ void peer_expert_phase(const Args& a, int layer, LAS unsigned char* lds, int G, int bid) {
;     int tid = threadIdx.x; asm volatile("" : "+v"(tid)); const int lane = tid & 63; const int wave = __builtin_amdgcn_readfirstlane(tid >> 6);
;     size_t wz_ = 0; asm volatile("" : "+s"(wz_)); unsigned char* ws = a.ws + wz_;
;     const int gw = bid * NWAVES + wave, NGW = G * NWAVES;
;     const bf16* XN = (const bf16*)(ws + WS_XN); bf16* H = (bf16*)(ws + WS_H);
;     const int* IDX = (const int*)(ws + WS_IDX); const float* GATE = (const float*)(ws + WS_GATE);
;     const unsigned char* PU = ws + WS_PU + (size_t)layer * SZ_PT; const unsigned char* PV = ws + WS_PV + (size_t)layer * SZ_PT;
;     const float* SCU = (const float*)(ws + WS_PSC) + layer * NEXP; const float* SCV = (const float*)(ws + WS_PSC) + (2 + layer) * NEXP;
;     const bool last = (layer == NLAYER - 1);
;     const float* gnext = last ? a.in[24] : a.in[17] + (layer + 1) * DM;
;     LAS unsigned char* X8 = lds + wave * 16384;
;     const int srot = (int)((xb_xcc_id() & 7u) * 4u);
; #pragma unroll 1
;     for (int tb = gw; tb < NTOK; tb += 4 * NGW) {
;         int ea[4], eb[4]; int pacc[4][16]; float xs[4];
; #pragma unroll
;         for (int i = 0; i < 4; ++i) { int tok = tb + i * NGW; const bool ok = tok < NTOK; tok = ok ? tok : tb; ea[i] = ok ? IDX[(size_t)tok * 128 + lane] : 0; eb[i] = ok ? IDX[(size_t)tok * 128 + 64 + lane] : 0;
; #pragma unroll
;             for (int c = 0; c < 16; ++c) pacc[i][c] = 0;
;             const u32x4* xr = (const u32x4*)(XN + (size_t)tok * DM) + lane; u32x4 xv[8]; float am = 0.f;
; #pragma unroll
;             for (int j = 0; j < 8; ++j) { xv[j] = xr[64 * j];
;                 am = fmaxf(am, fmaxf(fmaxf(fmaxf(fabsf(bflo(xv[j].x)), fabsf(bfhi(xv[j].x))), fmaxf(fabsf(bflo(xv[j].y)), fabsf(bfhi(xv[j].y)))), fmaxf(fmaxf(fabsf(bflo(xv[j].z)), fabsf(bfhi(xv[j].z))), fmaxf(fabsf(bflo(xv[j].w)), fabsf(bfhi(xv[j].w)))))); }
;             am = wave_max(am); const float qs = am > 0.f ? 127.0f / am : 0.f; xs[i] = am * (1.0f / 127.0f);
; #pragma unroll
;             for (int j = 0; j < 8; ++j) { u32x2 o; o.x = pk_i8(bflo(xv[j].x) * qs, bfhi(xv[j].x) * qs, bflo(xv[j].y) * qs, bfhi(xv[j].y) * qs); o.y = pk_i8(bflo(xv[j].z) * qs, bfhi(xv[j].z) * qs, bflo(xv[j].w) * qs, bfhi(xv[j].w) * qs);
.LBB0_1195:
	s_cmp_lt_i32 s90, 9
	s_cselect_b64 s[36:37], -1, 0
	s_and_b64 s[4:5], s[36:37], s[4:5]
	s_andn2_b64 vcc, exec, s[4:5]
	s_cbranch_vccnz .LBB0_1254
	s_load_dword s10, s[0:1], 0xe0
	s_mov_b32 s2, s94
	s_mov_b64 s[6:7], 0
	s_waitcnt lgkmcnt(0)
	s_waitcnt vmcnt(0)
	v_mov_b32_e32 v2, v0
	s_lshl_b32 s2, s2, 3
	v_readfirstlane_b32 s6, v2
	s_ashr_i32 s6, s6, 6
	s_mov_b64 s[4:5], 0
	s_add_i32 s38, s6, s2
	s_cmpk_gt_i32 s38, 0x1fff
	s_getreg_b32 s28, hwreg(HW_REG_XCC_ID, 0, 4)
	s_cbranch_scc1 .LBB0_1254
	s_load_dwordx2 s[8:9], s[0:1], 0xd0
	s_load_dwordx2 s[12:13], s[0:1], 0x88
	v_and_b32_e32 v1, 63, v2
	v_mbcnt_lo_u32_b32 v3, -1, 0
	v_lshlrev_b32_e32 v10, 4, v1
	s_waitcnt lgkmcnt(0)
	s_add_u32 s14, s8, s4
	s_addc_u32 s15, s9, s5
	s_lshl_b32 s2, s10, 3
	s_add_u32 s40, s14, 0x21482000
	s_addc_u32 s41, s15, 0
	s_add_u32 s33, s14, 0x11440000
	s_addc_u32 s72, s15, 0
	s_add_u32 s73, s14, 0x19440000
	s_addc_u32 s74, s15, 0
	s_add_u32 s42, s14, 0x21440000
	s_addc_u32 s43, s15, 0
	s_add_u32 s46, s14, 0x21460000
	s_addc_u32 s47, s15, 0
	s_add_u32 s48, s12, 0x4000
	s_addc_u32 s49, s13, 0
	s_lshl_b32 s4, s6, 14
	v_mov_b32_e32 v11, 0
	v_mbcnt_hi_u32_b32 v3, -1, v3
	s_add_i32 s29, s4, 0
	v_lshl_add_u64 v[4:5], s[14:15], 0, v[10:11]
	s_mov_b64 s[4:5], 0x29482000
	v_and_b32_e32 v8, 64, v3
	v_lshl_add_u64 v[12:13], v[4:5], 0, s[4:5]
	v_add_u32_e32 v4, 64, v8
	v_xor_b32_e32 v5, 32, v3
	v_cmp_lt_i32_e32 vcc, v5, v4
	v_lshlrev_b32_e32 v10, 2, v1
	s_mov_b64 s[4:5], 0x45482000
	v_cndmask_b32_e32 v5, v3, v5, vcc
	v_lshlrev_b32_e32 v36, 2, v5
	v_xor_b32_e32 v5, 16, v3
	v_cmp_lt_i32_e32 vcc, v5, v4
	v_and_b32_e32 v7, 7, v2
	v_lshlrev_b32_e32 v6, 5, v7
	v_cndmask_b32_e32 v5, v3, v5, vcc
	v_lshlrev_b32_e32 v37, 2, v5
	v_xor_b32_e32 v5, 8, v3
	v_cmp_lt_i32_e32 vcc, v5, v4
	v_bfe_u32 v24, v2, 3, 3
	v_lshlrev_b32_e32 v42, 4, v7
	v_cndmask_b32_e32 v5, v3, v5, vcc
	v_lshlrev_b32_e32 v38, 2, v5
	v_xor_b32_e32 v5, 4, v3
	v_cmp_lt_i32_e32 vcc, v5, v4
	s_add_u32 s75, s14, 0x56992000
	s_addc_u32 s76, s15, 0
	v_cndmask_b32_e32 v5, v3, v5, vcc
	v_lshlrev_b32_e32 v39, 2, v5
	v_xor_b32_e32 v5, 2, v3
	v_cmp_lt_i32_e32 vcc, v5, v4
	s_add_u32 s77, s14, 0x54992000
	v_lshlrev_b32_e32 v9, 3, v1
	v_cndmask_b32_e32 v5, v3, v5, vcc
	v_lshlrev_b32_e32 v40, 2, v5
	v_xor_b32_e32 v5, 1, v3
	v_cmp_lt_i32_e32 vcc, v5, v4
	s_addc_u32 s78, s15, 0
	s_and_b32 s28, s28, 15
	v_cndmask_b32_e32 v4, v3, v5, vcc
	v_lshlrev_b32_e32 v41, 2, v4
	v_lshl_add_u64 v[4:5], s[14:15], 0, v[10:11]
	v_lshl_add_u64 v[14:15], v[4:5], 0, s[4:5]
	v_lshlrev_b32_e32 v3, 2, v3
	s_movk_i32 s4, 0x100
	v_and_or_b32 v44, v3, s4, v6
	s_mov_b64 s[4:5], 0x4ad82000
	v_lshl_add_u64 v[16:17], v[4:5], 0, s[4:5]
	s_mov_b64 s[4:5], 0x45882000
	v_lshlrev_b32_e32 v10, 6, v7
	v_and_b32_e32 v3, 32, v2
	v_lshl_add_u64 v[18:19], v[4:5], 0, s[4:5]
	v_lshl_add_u64 v[4:5], s[48:49], 0, v[10:11]
	v_and_b32_e32 v10, 56, v2
	v_cmp_eq_u32_e64 s[4:5], 0, v3
	v_and_b32_e32 v3, 16, v2
	v_and_b32_e32 v2, 8, v2
	v_mov_b32_e32 v7, v11
	v_lshl_add_u64 v[20:21], v[4:5], 0, v[10:11]
	v_cmp_eq_u32_e64 s[6:7], 0, v3
	v_cmp_eq_u32_e64 s[8:9], 0, v2
	v_lshl_add_u64 v[2:3], s[40:41], 0, v[6:7]
	v_lshlrev_b32_e32 v10, 2, v24
	v_lshl_add_u64 v[22:23], v[2:3], 0, v[10:11]
	v_or_b32_e32 v2, v8, v24
	v_lshlrev_b32_e32 v10, 2, v2
	s_mov_b32 s51, 0
	v_add_u32_e32 v43, s29, v42
	s_lshl_b32 s79, s10, 5
	v_or_b32_e32 v45, 32, v10
	v_or_b32_e32 v46, 64, v10
	v_or_b32_e32 v47, 0x60, v10
	v_or_b32_e32 v48, 0x80, v10
	v_or_b32_e32 v49, 0xa0, v10
	v_or_b32_e32 v50, 0xc0, v10
	v_or_b32_e32 v51, 0xe0, v10
	v_cmp_gt_u32_e64 s[10:11], 8, v1
	v_cmp_eq_u32_e64 s[12:13], 1, v24
	v_cmp_eq_u32_e64 s[14:15], 2, v24
	v_cmp_eq_u32_e64 s[16:17], 3, v24
	v_cmp_eq_u32_e64 s[18:19], 4, v24
	v_cmp_eq_u32_e64 s[20:21], 5, v24
	v_cmp_eq_u32_e64 s[22:23], 6, v24
	v_cmp_eq_u32_e64 s[24:25], 7, v24
	s_mov_b32 s80, 0
	s_movk_i32 s81, 0x1000
	s_mov_b32 s82, 0x42fe0000
	s_mov_b32 s83, 0xc0c0400
	s_mov_b32 s84, 0x5040100
	v_mov_b32_e32 v52, 0x358637bd
	s_mov_b32 s85, 0xf800000
	v_mov_b32_e32 v53, 0x260
	s_mov_b32 s86, 0x3f200000
	s_mov_b32 s87, 0x3fb8aa3b
	s_mov_b32 s88, 0xc2ce8ed0
	s_mov_b32 s89, 0x42b17218
	v_mov_b32_e32 v54, 0x3ca908c9
	s_brev_b32 s90, -2
	s_mov_b32 s91, 0x5010400
	s_mov_b32 s92, 0x7030602
	s_mov_b32 s93, 0x7060302
	v_add_u32_e32 v55, s29, v9
	v_mov_b32_e32 v56, 0x7f800000
	s_branch .LBB0_1199

; #define LAS __attribute__((address_space(3)))
; __device__ __forceinline__ void peer_expert_phase(const Args& a, int layer, LAS unsigned char* lds, int G, int bid) {
;     int tid = threadIdx.x; asm volatile("" : "+v"(tid)); const int lane = tid & 63; const int wave = __builtin_amdgcn_readfirstlane(tid >> 6);
;     size_t wz_ = 0; asm volatile("" : "+s"(wz_)); unsigned char* ws = a.ws + wz_;
;     const int gw = bid * NWAVES + wave, NGW = G * NWAVES;
;     const bf16* XN = (const bf16*)(ws + WS_XN); bf16* H = (bf16*)(ws + WS_H);
;     const int* IDX = (const int*)(ws + WS_IDX); const float* GATE = (const float*)(ws + WS_GATE);
;     const unsigned char* PU = ws + WS_PU + (size_t)layer * SZ_PT; const unsigned char* PV = ws + WS_PV + (size_t)layer * SZ_PT;
;     const float* SCU = (const float*)(ws + WS_PSC) + layer * NEXP; const float* SCV = (const float*)(ws + WS_PSC) + (2 + layer) * NEXP;
;     const bool last = (layer == NLAYER - 1);
;     const float* gnext = last ? a.in[24] : a.in[17] + (layer + 1) * DM;
;     LAS unsigned char* X8 = lds + wave * 16384;
;     const int srot = (int)((xb_xcc_id() & 7u) * 4u);
; #pragma unroll 1
;     for (int tb = gw; tb < NTOK; tb += 4 * NGW) {
;         int ea[4], eb[4]; int pacc[4][16]; float xs[4];
; #pragma unroll
;         for (int i = 0; i < 4; ++i) { int tok = tb + i * NGW; const bool ok = tok < NTOK; tok = ok ? tok : tb; ea[i] = ok ? IDX[(size_t)tok * 128 + lane] : 0; eb[i] = ok ? IDX[(size_t)tok * 128 + 64 + lane] : 0;
; #pragma unroll
;             for (int c = 0; c < 16; ++c) pacc[i][c] = 0;
;             const u32x4* xr = (const u32x4*)(XN + (size_t)tok * DM) + lane; u32x4 xv[8]; float am = 0.f;
; #pragma unroll
;             for (int j = 0; j < 8; ++j) { xv[j] = xr[64 * j];
;                 am = fmaxf(am, fmaxf(fmaxf(fmaxf(fabsf(bflo(xv[j].x)), fabsf(bfhi(xv[j].x))), fmaxf(fabsf(bflo(xv[j].y)), fabsf(bfhi(xv[j].y)))), fmaxf(fmaxf(fabsf(bflo(xv[j].z)), fabsf(bfhi(xv[j].z))), fmaxf(fabsf(bflo(xv[j].w)), fabsf(bfhi(xv[j].w)))))); }
;             am = wave_max(am); const float qs = am > 0.f ? 127.0f / am : 0.f; xs[i] = am * (1.0f / 127.0f);
; #pragma unroll
;             for (int j = 0; j < 8; ++j) { u32x2 o; o.x = pk_i8(bflo(xv[j].x) * qs, bfhi(xv[j].x) * qs, bflo(xv[j].y) * qs, bfhi(xv[j].y) * qs); o.y = pk_i8(bflo(xv[j].z) * qs, bfhi(xv[j].z) * qs, bflo(xv[j].w) * qs, bfhi(xv[j].w) * qs);
.LBB0_2256:
	s_cmp_gt_i32 s90, 16
	s_cselect_b64 s[2:3], -1, 0
	s_xor_b64 s[4:5], s[4:5], -1
	s_or_b64 s[2:3], s[2:3], s[4:5]
	s_and_b64 vcc, exec, s[2:3]
	s_cbranch_vccnz .LBB0_2312
	s_load_dword s6, s[0:1], 0xe0
	s_mov_b64 s[2:3], 0
	s_waitcnt lgkmcnt(0)
	s_lshl_b32 s3, s94, 3
	v_readfirstlane_b32 s2, v0
	s_ashr_i32 s2, s2, 6
	s_mov_b64 s[4:5], 0
	s_add_i32 s26, s2, s3
	s_cmpk_gt_i32 s26, 0x1fff
	s_getreg_b32 s22, hwreg(HW_REG_XCC_ID, 0, 4)
	s_cbranch_scc1 .LBB0_2312
	s_load_dwordx2 s[8:9], s[0:1], 0xd0
	s_load_dwordx4 s[28:31], s[0:1], 0xc0
	s_waitcnt vmcnt(0)
	v_and_b32_e32 v28, 63, v0
	v_mbcnt_lo_u32_b32 v1, -1, 0
	v_lshlrev_b32_e32 v2, 4, v28
	s_waitcnt lgkmcnt(0)
	s_add_u32 s0, s8, s4
	s_addc_u32 s1, s9, s5
	s_lshl_b32 s33, s6, 3
	s_add_u32 s34, s0, 0x21482000
	s_addc_u32 s35, s1, 0
	s_add_u32 s62, s0, 0x15440000
	s_addc_u32 s63, s1, 0
	s_add_u32 s64, s0, 0x1d440000
	s_addc_u32 s65, s1, 0
	s_add_u32 s36, s0, 0x21450000
	s_addc_u32 s37, s1, 0
	s_add_u32 s38, s0, 0x21470000
	s_addc_u32 s39, s1, 0
	s_lshl_b32 s2, s2, 14
	v_mov_b32_e32 v3, 0
	v_mbcnt_hi_u32_b32 v1, -1, v1
	s_add_i32 s23, s2, 0
	v_lshl_add_u64 v[4:5], s[0:1], 0, v[2:3]
	s_mov_b64 s[2:3], 0x29482000
	v_and_b32_e32 v6, 64, v1
	v_lshl_add_u64 v[8:9], v[4:5], 0, s[2:3]
	v_add_u32_e32 v2, 64, v6
	v_xor_b32_e32 v4, 32, v1
	v_cmp_lt_i32_e32 vcc, v4, v2
	v_bfe_u32 v18, v0, 3, 3
	v_lshlrev_b32_e32 v7, 3, v28
	v_cndmask_b32_e32 v4, v1, v4, vcc
	v_lshlrev_b32_e32 v29, 2, v4
	v_xor_b32_e32 v4, 16, v1
	v_cmp_lt_i32_e32 vcc, v4, v2
	s_and_b32 s22, s22, 15
	s_mov_b32 s41, 0
	v_cndmask_b32_e32 v4, v1, v4, vcc
	v_lshlrev_b32_e32 v30, 2, v4
	v_xor_b32_e32 v4, 8, v1
	v_cmp_lt_i32_e32 vcc, v4, v2
	s_lshl_b32 s66, s6, 5
	v_cmp_gt_u32_e64 s[6:7], 8, v28
	v_cndmask_b32_e32 v4, v1, v4, vcc
	v_lshlrev_b32_e32 v31, 2, v4
	v_xor_b32_e32 v4, 4, v1
	v_cmp_lt_i32_e32 vcc, v4, v2
	v_cmp_eq_u32_e64 s[8:9], 1, v18
	v_cmp_eq_u32_e64 s[10:11], 2, v18
	v_cndmask_b32_e32 v4, v1, v4, vcc
	v_lshlrev_b32_e32 v32, 2, v4
	v_xor_b32_e32 v4, 2, v1
	v_cmp_lt_i32_e32 vcc, v4, v2
	v_cmp_eq_u32_e64 s[12:13], 3, v18
	v_cmp_eq_u32_e64 s[14:15], 4, v18
	v_cndmask_b32_e32 v4, v1, v4, vcc
	v_lshlrev_b32_e32 v33, 2, v4
	v_xor_b32_e32 v4, 1, v1
	v_cmp_lt_i32_e32 vcc, v4, v2
	v_cmp_eq_u32_e64 s[16:17], 5, v18
	v_cmp_eq_u32_e64 s[18:19], 6, v18
	v_cndmask_b32_e32 v2, v1, v4, vcc
	v_lshlrev_b32_e32 v34, 2, v2
	v_lshlrev_b32_e32 v2, 2, v28
	v_lshl_add_u64 v[4:5], s[0:1], 0, v[2:3]
	s_mov_b64 s[0:1], 0x45482000
	v_and_b32_e32 v2, 7, v0
	v_lshl_add_u64 v[10:11], v[4:5], 0, s[0:1]
	v_lshlrev_b32_e32 v35, 4, v2
	v_lshlrev_b32_e32 v2, 5, v2
	v_lshlrev_b32_e32 v1, 2, v1
	s_movk_i32 s0, 0x100
	v_and_or_b32 v37, v1, s0, v2
	s_mov_b64 s[0:1], 0x4af82000
	v_lshl_add_u64 v[12:13], v[4:5], 0, s[0:1]
	s_mov_b64 s[0:1], 0x45882000
	v_and_b32_e32 v1, 32, v0
	v_lshl_add_u64 v[14:15], v[4:5], 0, s[0:1]
	v_cmp_eq_u32_e64 s[0:1], 0, v1
	v_and_b32_e32 v1, 16, v0
	v_and_b32_e32 v0, 8, v0
	v_cmp_eq_u32_e64 s[2:3], 0, v1
	v_cmp_eq_u32_e64 s[4:5], 0, v0
	v_lshl_add_u64 v[0:1], s[34:35], 0, v[2:3]
	v_lshlrev_b32_e32 v2, 2, v18
	v_lshl_add_u64 v[16:17], v[0:1], 0, v[2:3]
	v_or_b32_e32 v0, v6, v18
	v_lshlrev_b32_e32 v38, 2, v0
	v_add_u32_e32 v36, s23, v35
	v_or_b32_e32 v39, 32, v38
	v_or_b32_e32 v40, 64, v38
	v_or_b32_e32 v41, 0x60, v38
	v_or_b32_e32 v42, 0x80, v38
	v_or_b32_e32 v43, 0xa0, v38
	v_or_b32_e32 v44, 0xc0, v38
	v_or_b32_e32 v45, 0xe0, v38
	v_cmp_eq_u32_e64 s[20:21], 7, v18
	s_mov_b32 s67, 0
	s_movk_i32 s68, 0x1000
	s_mov_b32 s69, 0x42fe0000
	s_mov_b32 s70, 0xc0c0400
	s_mov_b32 s71, 0x5040100
	v_add_u32_e32 v46, s23, v7
	v_mov_b32_e32 v47, 0x358637bd
	s_mov_b32 s72, 0xf800000
	v_mov_b32_e32 v48, 0x260
	s_mov_b32 s73, 0x3f200000
	s_mov_b32 s74, 0x3fb8aa3b
	s_mov_b32 s75, 0xc2ce8ed0
	s_mov_b32 s76, 0x42b17218
	v_mov_b32_e32 v49, 0x3ca908c9
	s_brev_b32 s77, -2
	s_mov_b32 s78, 0x5010400
	s_mov_b32 s79, 0x7030602
	s_mov_b32 s80, 0x7060302
	v_mov_b32_e32 v50, 0x7f800000
	s_branch .LBB0_2260
